# union: v50 (nt streaming hints) + next-unit Q prefetch + P5 epilogue de-serialised + K-tile DMA gather shape
# speedup vs baseline: 1.0031x; 1.0010x over previous
.Lqpf_done:
	s_waitcnt lgkmcnt(0)
	v_add_u32_e32 v0, s11, v213
	ds_read_b128 v[36:39], v0 offset:128
	ds_read_b128 v[40:43], v0 offset:160
	s_add_u32 s10, s8, s90
	s_addc_u32 s11, s9, s91
	s_lshl_b32 s14, s42, 12
	s_waitcnt lgkmcnt(1)
	v_rcp_f32_e32 v2, v36
	v_rcp_f32_e32 v44, v37
	v_rcp_f32_e32 v45, v38
	v_rcp_f32_e32 v46, v39
	s_waitcnt lgkmcnt(0)
	v_rcp_f32_e32 v47, v40
	ds_read_b128 v[36:39], v0 offset:192
	v_rcp_f32_e32 v48, v41
	v_rcp_f32_e32 v49, v42
	v_rcp_f32_e32 v50, v43
	ds_read_b128 v[40:43], v0 offset:224
	s_waitcnt lgkmcnt(1)
	v_rcp_f32_e32 v0, v36
	v_rcp_f32_e32 v36, v37
	v_rcp_f32_e32 v37, v38
	v_rcp_f32_e32 v38, v39
	s_waitcnt lgkmcnt(0)
	v_rcp_f32_e32 v39, v40
	v_rcp_f32_e32 v40, v41
	v_rcp_f32_e32 v41, v42
	v_rcp_f32_e32 v42, v43
	s_add_i32 s14, s14, 0
	v_lshlrev_b32_e32 v43, 1, v207
	v_mul_f32_e32 v4, v4, v2
	v_mul_f32_e32 v2, v20, v2
	v_add3_u32 v43, s14, v202, v43
	v_cvt_pk_bf16_f32 v2, v2, s0
	ds_write_b16 v43, v2 offset:64
	v_mul_f32_e32 v2, v5, v44
	v_cvt_pk_bf16_f32 v2, v2, s0
	ds_write_b16 v43, v2 offset:128
	v_mul_f32_e32 v2, v21, v44
	v_cvt_pk_bf16_f32 v2, v2, s0
	ds_write_b16 v43, v2 offset:192
	v_mul_f32_e32 v2, v6, v45
	v_cvt_pk_bf16_f32 v2, v2, s0
	ds_write_b16 v43, v2 offset:256
	v_mul_f32_e32 v2, v22, v45
	v_cvt_pk_bf16_f32 v2, v2, s0
	ds_write_b16 v43, v2 offset:320
	v_mul_f32_e32 v2, v7, v46
	v_cvt_pk_bf16_f32 v2, v2, s0
	ds_write_b16 v43, v2 offset:384
	v_mul_f32_e32 v2, v23, v46
	v_cvt_pk_bf16_f32 v2, v2, s0
	ds_write_b16 v43, v2 offset:448
	v_mul_f32_e32 v2, v8, v47
	v_cvt_pk_bf16_f32 v2, v2, s0
	ds_write_b16 v43, v2 offset:1024
	v_mul_f32_e32 v2, v24, v47
	v_cvt_pk_bf16_f32 v2, v2, s0
	ds_write_b16 v43, v2 offset:1088
	v_mul_f32_e32 v2, v9, v48
	v_cvt_pk_bf16_f32 v2, v2, s0
	ds_write_b16 v43, v2 offset:1152
	v_mul_f32_e32 v2, v25, v48
	v_cvt_pk_bf16_f32 v2, v2, s0
	ds_write_b16 v43, v2 offset:1216
	v_mul_f32_e32 v2, v10, v49
	v_cvt_pk_bf16_f32 v2, v2, s0
	ds_write_b16 v43, v2 offset:1280
	v_mul_f32_e32 v2, v26, v49
	v_cvt_pk_bf16_f32 v2, v2, s0
	ds_write_b16 v43, v2 offset:1344
	v_mul_f32_e32 v2, v11, v50
	v_cvt_pk_bf16_f32 v2, v2, s0
	ds_write_b16 v43, v2 offset:1408
	v_mul_f32_e32 v2, v27, v50
	v_cvt_pk_bf16_f32 v2, v2, s0
	ds_write_b16 v43, v2 offset:1472
	v_mul_f32_e32 v2, v12, v0
	v_mul_f32_e32 v0, v28, v0
	v_cvt_pk_bf16_f32 v0, v0, s0
	ds_write_b16 v43, v0 offset:2112
	v_mul_f32_e32 v0, v13, v36
	v_cvt_pk_bf16_f32 v0, v0, s0
	ds_write_b16 v43, v0 offset:2176
	v_mul_f32_e32 v0, v29, v36
	v_cvt_pk_bf16_f32 v0, v0, s0
	ds_write_b16 v43, v0 offset:2240
	v_mul_f32_e32 v0, v14, v37
	v_cvt_pk_bf16_f32 v0, v0, s0
	ds_write_b16 v43, v0 offset:2304
	v_mul_f32_e32 v0, v30, v37
	v_cvt_pk_bf16_f32 v0, v0, s0
	ds_write_b16 v43, v0 offset:2368
	v_mul_f32_e32 v0, v15, v38
	v_cvt_pk_bf16_f32 v0, v0, s0
	ds_write_b16 v43, v0 offset:2432
	v_mul_f32_e32 v0, v31, v38
	v_cvt_pk_bf16_f32 v0, v0, s0
	ds_write_b16 v43, v0 offset:2496
	v_mul_f32_e32 v0, v16, v39
	v_cvt_pk_bf16_f32 v0, v0, s0
	ds_write_b16 v43, v0 offset:3072
	v_mul_f32_e32 v0, v32, v39
	v_cvt_pk_bf16_f32 v0, v0, s0
	ds_write_b16 v43, v0 offset:3136
	v_mul_f32_e32 v0, v17, v40
	v_cvt_pk_bf16_f32 v0, v0, s0
	ds_write_b16 v43, v0 offset:3200
	v_mul_f32_e32 v0, v33, v40
	v_cvt_pk_bf16_f32 v0, v0, s0
	ds_write_b16 v43, v0 offset:3264
	v_mul_f32_e32 v0, v18, v41
	v_cvt_pk_bf16_f32 v0, v0, s0
	ds_write_b16 v43, v0 offset:3328
	v_mul_f32_e32 v0, v34, v41
	v_cvt_pk_bf16_f32 v0, v0, s0
	ds_write_b16 v43, v0 offset:3392
	v_mul_f32_e32 v0, v19, v42
	v_cvt_pk_bf16_f32 v0, v0, s0
	v_cvt_pk_bf16_f32 v2, v2, s0
	ds_write_b16 v43, v0 offset:3456
	v_mul_f32_e32 v0, v35, v42
	v_cvt_pk_bf16_f32 v4, v4, s0
	ds_write_b16 v43, v2 offset:2048
	v_cvt_pk_bf16_f32 v0, v0, s0
	s_add_u32 s10, s10, vcc_lo
	v_lshlrev_b32_e32 v2, 1, v200
	ds_write_b16 v43, v4
	ds_write_b16 v43, v0 offset:3520
	s_addc_u32 s11, s11, vcc_hi
	v_add_u32_e32 v0, s14, v2
	s_waitcnt lgkmcnt(0)
	v_lshl_add_u64 v[8:9], s[10:11], 0, v[2:3]
	v_add_u32_e32 v2, v0, v203
	ds_read_b128 v[4:7], v2
	v_lshlrev_b32_e32 v2, 1, v196
	v_lshl_add_u64 v[12:13], v[8:9], 0, v[2:3]
	v_add_u32_e32 v2, v0, v204
	ds_read_b128 v[8:11], v2
	s_waitcnt lgkmcnt(1)
	global_store_dwordx4 v[12:13], v[4:7], off
	v_add_u32_e32 v2, v0, v205
	v_add_u32_e32 v0, v0, v206
	v_add_co_u32_e32 v4, vcc, 0x6000, v12
	s_nop 1
	v_addc_co_u32_e32 v5, vcc, 0, v13, vcc
	s_waitcnt lgkmcnt(0)
	global_store_dwordx4 v[4:5], v[8:11], off
	ds_read_b128 v[4:7], v2
	ds_read_b128 v[8:11], v0
	v_add_co_u32_e32 v14, vcc, 0xc000, v12
	s_nop 1
	v_addc_co_u32_e32 v15, vcc, 0, v13, vcc
	s_waitcnt lgkmcnt(1)
	global_store_dwordx4 v[14:15], v[4:7], off
	s_nop 1
	v_add_co_u32_e32 v4, vcc, 0x12000, v12
	s_nop 1
	v_addc_co_u32_e32 v5, vcc, 0, v13, vcc
	s_waitcnt lgkmcnt(0)
	global_store_dwordx4 v[4:5], v[8:11], off
	s_waitcnt lgkmcnt(0)
	s_barrier
	v_mbcnt_lo_u32_b32 v0, -1, 0
	v_mbcnt_hi_u32_b32 v0, -1, v0
	v_lshrrev_b32_e32 v2, 5, v0
	v_and_b32_e32 v0, 31, v0
	v_lshlrev_b32_e32 v0, 4, v0
	v_lshl_add_u32 v210, v2, 10, v0

.LBB0_334:
	s_and_b64 vcc, exec, s[60:61]
	s_cbranch_vccz .LBB0_242
	v_readlane_b32 s10, v254, 20
	s_add_u32 s10, s10, s56
	v_readlane_b32 s11, v254, 19
	s_addc_u32 s11, s11, s57
	s_add_u32 s14, s10, s58
	s_addc_u32 s15, s11, s59
	s_lshl_b64 s[90:91], s[54:55], 1
	s_add_u32 s10, s73, s90
	v_readfirstlane_b32 s11, v235
	s_addc_u32 s44, s75, s91
	s_lshr_b32 s42, s11, 6
	s_lshl_b32 s53, s42, 5
	s_mul_i32 s54, s42, 0xc000
	s_mul_hi_u32 s55, s53, 0x600
	s_lshl_b64 vcc, s[54:55], 1
	s_add_u32 s62, s10, vcc_lo
	s_addc_u32 s63, s44, vcc_hi
	s_lshl_b32 s10, s42, 4
	v_mbcnt_lo_u32_b32 v36, -1, 0
	v_mbcnt_hi_u32_b32 v36, -1, v36
	v_and_b32_e32 v37, 15, v36
	v_mul_u32_u24_e32 v37, 0x300, v37
	v_lshrrev_b32_e32 v38, 4, v36
	v_lshl_add_u32 v37, v38, 4, v37
	s_and_b32 s53, s42, 3
	s_mul_i32 s53, s53, 0x3000
	s_lshr_b32 s54, s42, 2
	s_lshl_b32 s54, s54, 6
	s_add_i32 s53, s53, s54
	v_add_u32_e32 v165, s53, v37
	v_bfe_u32 v37, v36, 4, 1
	v_lshlrev_b32_e32 v37, 10, v37
	v_lshrrev_b32_e32 v38, 5, v36
	v_lshl_add_u32 v37, v38, 8, v37
	v_and_b32_e32 v38, 15, v36
	v_lshl_add_u32 v210, v38, 4, v37
	v_and_or_b32 v0, s10, 48, v201
	s_lshr_b32 s10, s11, 3
	s_and_b32 s10, s10, 0x1fffffe0
	s_lshl_b32 s44, s42, 10
	v_mov_b32_e32 v2, s10
	s_movk_i32 s10, 0x180
	s_cmp_lg_u32 0, -1
	v_mad_u32_u24 v0, v0, s10, v2
	s_cselect_b32 s10, 0, 0
	s_add_i32 s70, s44, s10
	v_or_b32_e32 v0, v0, v209
	s_add_i32 s10, s70, 0xc000
	s_mov_b32 m0, s70
	s_nop 0
	global_load_lds_dwordx4 v165, s[88:89]
	v_lshlrev_b32_e32 v164, 1, v0
	s_mov_b32 m0, s10
	s_nop 0
	global_load_lds_dwordx4 v164, s[14:15]
	s_add_u32 s54, s88, 0xc000
	s_addc_u32 s55, s89, 0
	s_add_i32 s71, s70, 0x2000
	s_mov_b32 m0, s71
	s_nop 0
	global_load_lds_dwordx4 v165, s[54:55]
	s_cmp_lg_u32 s32, 0
	s_cbranch_scc1 .Lqpf_skip
	global_load_dwordx4 v[140:143], v217, s[62:63]
	global_load_dwordx4 v[128:131], v217, s[62:63] offset:32
	global_load_dwordx4 v[136:139], v217, s[62:63] offset:64
	global_load_dwordx4 v[132:135], v217, s[62:63] offset:96
.Lqpf_skip:
	s_add_u32 s64, s88, 0x18000
	s_addc_u32 s65, s89, 0
	s_add_i32 s76, s70, 0x4000
	s_add_u32 s62, s88, 0x24000
	s_mov_b32 m0, s76
	s_nop 0
	global_load_lds_dwordx4 v165, s[64:65]
	s_addc_u32 s63, s89, 0
	s_add_i32 s77, s70, 0x6000
	s_mov_b32 m0, s77
	s_nop 0
	global_load_lds_dwordx4 v165, s[62:63]
	s_add_u32 s62, s14, 0xc000
	s_addc_u32 s63, s15, 0
	s_add_i32 s78, s70, 0xe000
	s_mov_b32 m0, s78
	s_nop 0
	global_load_lds_dwordx4 v164, s[62:63]
	s_add_u32 s62, s88, 0x30000
	s_addc_u32 s63, s89, 0
	s_add_i32 s79, s70, 0x8000
	s_mov_b32 m0, s79
	s_nop 0
	global_load_lds_dwordx4 v165, s[62:63]
	s_add_u32 s62, s88, 0x3c000
	s_addc_u32 s63, s89, 0
	s_add_i32 s85, s70, 0xa000
	s_mov_b32 m0, s85
	s_nop 0
	global_load_lds_dwordx4 v165, s[62:63]
	s_add_u32 s62, s14, 0x18000
	s_addc_u32 s63, s15, 0
	s_add_i32 s92, s70, 0x10000
	s_mov_b32 m0, s92
	s_nop 0
	global_load_lds_dwordx4 v164, s[62:63]
	s_add_u32 s62, s14, 0x24000
	s_addc_u32 s63, s15, 0
	s_add_i32 s93, s70, 0x12000
	s_mov_b32 m0, s93
	s_nop 0
	global_load_lds_dwordx4 v164, s[62:63]
	s_waitcnt vmcnt(7) lgkmcnt(0)
	s_barrier
	s_waitcnt vmcnt(22)
	ds_read_b128 v[36:39], v210
	s_waitcnt vmcnt(21)
	ds_read_b128 v[40:43], v210 offset:2048
	s_mov_b32 s53, s52
	s_mov_b32 s54, s52
	s_mov_b32 s55, s52
	s_mov_b32 s56, s52
	s_mov_b32 s57, s52
	s_mov_b32 s58, s52
	s_mov_b32 s59, s52
	s_mov_b32 s60, s52
	s_mov_b32 s61, s52
	s_mov_b32 s62, s52
	s_mov_b32 s63, s52
	s_mov_b32 s64, s52
	s_mov_b32 s65, s52
	s_mov_b32 s66, s52
	s_mov_b32 s67, s52
	s_waitcnt vmcnt(13)
	v_mov_b64_e32 v[4:5], s[52:53]
	v_mov_b64_e32 v[6:7], s[54:55]
	v_mov_b64_e32 v[8:9], s[56:57]
	v_mov_b64_e32 v[10:11], s[58:59]
	v_mov_b64_e32 v[12:13], s[60:61]
	v_mov_b64_e32 v[14:15], s[62:63]
	v_mov_b64_e32 v[16:17], s[64:65]
	v_mov_b64_e32 v[18:19], s[66:67]
	v_mov_b32_e32 v148, 0
	v_mov_b32_e32 v2, 0
	v_mov_b32_e32 v72, 0
	s_mov_b32 s53, -5
	s_waitcnt lgkmcnt(1)
	v_mfma_f32_32x32x16_bf16 v[20:35], v[36:39], v[140:143], v[4:19]
	s_mov_b64 s[54:55], 0
	v_mov_b32_e32 v73, 0
	v_mov_b32_e32 v149, v148
	v_mov_b32_e32 v150, v148
	v_mov_b32_e32 v151, v148
	s_waitcnt lgkmcnt(0)
	v_mfma_f32_32x32x16_bf16 v[4:19], v[40:43], v[140:143], v[4:19]
	ds_read_b128 v[36:39], v210 offset:512
	ds_read_b128 v[40:43], v210 offset:2560
	s_waitcnt lgkmcnt(1)
	v_mfma_f32_32x32x16_bf16 v[20:35], v[36:39], v[128:131], v[20:35]
	s_waitcnt lgkmcnt(0)
	v_mfma_f32_32x32x16_bf16 v[4:19], v[40:43], v[128:131], v[4:19]
	ds_read_b128 v[36:39], v210 offset:4096
	ds_read_b128 v[40:43], v210 offset:6144
	s_waitcnt lgkmcnt(1)
	v_mfma_f32_32x32x16_bf16 v[20:35], v[36:39], v[136:139], v[20:35]
	s_waitcnt lgkmcnt(0)
	v_mfma_f32_32x32x16_bf16 v[4:19], v[40:43], v[136:139], v[4:19]
	ds_read_b128 v[36:39], v210 offset:4608
	ds_read_b128 v[40:43], v210 offset:6656
	s_waitcnt lgkmcnt(1)
	v_mfma_f32_32x32x16_bf16 v[20:35], v[36:39], v[132:135], v[20:35]
	s_waitcnt lgkmcnt(0)
	v_mfma_f32_32x32x16_bf16 v[4:19], v[40:43], v[132:135], v[4:19]
	s_nop 15
	s_nop 7
	s_waitcnt vmcnt(4) lgkmcnt(0)
	s_barrier
	ds_read_b128 v[68:71], v210 offset:8192
	ds_read_b128 v[160:163], v210 offset:10240
	ds_read_b128 v[156:159], v210 offset:8704
	ds_read_b128 v[112:115], v210 offset:10752
	ds_read_b128 v[152:155], v210 offset:12288
	ds_read_b128 v[104:107], v210 offset:14336
	ds_read_b128 v[108:111], v210 offset:12800
	ds_read_b128 v[100:103], v210 offset:14848
	s_nop 1
	v_exp_f32_e32 v52, v20
	v_exp_f32_e32 v53, v21
	v_exp_f32_e32 v54, v22
	v_exp_f32_e32 v55, v23
	v_exp_f32_e32 v56, v24
	v_exp_f32_e32 v57, v25
	v_exp_f32_e32 v58, v26
	v_exp_f32_e32 v59, v27
	v_exp_f32_e32 v60, v28
	v_exp_f32_e32 v61, v29
	v_exp_f32_e32 v62, v30
	v_exp_f32_e32 v63, v31
	v_exp_f32_e32 v64, v32
	v_exp_f32_e32 v65, v33
	v_exp_f32_e32 v66, v34
	v_exp_f32_e32 v67, v35
	v_exp_f32_e32 v36, v4
	v_exp_f32_e32 v37, v5
	v_exp_f32_e32 v38, v6
	v_exp_f32_e32 v39, v7
	v_exp_f32_e32 v40, v8
	v_exp_f32_e32 v41, v9
	v_exp_f32_e32 v42, v10
	v_exp_f32_e32 v43, v11
	v_mov_b32_e32 v44, v12
	v_mov_b32_e32 v45, v13
	v_mov_b32_e32 v46, v14
	v_mov_b32_e32 v47, v15
	v_mov_b32_e32 v48, v16
	v_mov_b32_e32 v49, v17
	v_mov_b32_e32 v50, v18
	v_mov_b32_e32 v51, v19
	s_waitcnt vmcnt(4) lgkmcnt(0)
	s_barrier
	v_mov_b32_e32 v4, 0
	v_mov_b32_e32 v5, v2
	v_mov_b32_e32 v6, v2
	v_mov_b32_e32 v7, v2
	v_mov_b32_e32 v8, v2
	v_mov_b32_e32 v9, v2
	v_mov_b32_e32 v10, v2
	v_mov_b32_e32 v11, v2
	v_mov_b32_e32 v12, v2
	v_mov_b32_e32 v13, v2
	v_mov_b32_e32 v14, v2
	v_mov_b32_e32 v15, v2
	v_mov_b32_e32 v16, v2
	v_mov_b32_e32 v17, v2
	v_mov_b32_e32 v18, v2
	v_mov_b32_e32 v19, v2
	v_mov_b32_e32 v20, 0
	v_mov_b32_e32 v21, v2
	v_mov_b32_e32 v22, v2
	v_mov_b32_e32 v23, v2
	v_mov_b32_e32 v24, v2
	v_mov_b32_e32 v25, v2
	v_mov_b32_e32 v26, v2
	v_mov_b32_e32 v27, v2
	v_mov_b32_e32 v28, v2
	v_mov_b32_e32 v29, v2
	v_mov_b32_e32 v30, v2
	v_mov_b32_e32 v31, v2
	v_mov_b32_e32 v32, v2
	v_mov_b32_e32 v33, v2
	v_mov_b32_e32 v34, v2
	v_mov_b32_e32 v35, v2

.LBB0_525:
	v_lshl_add_u32 v138, s71, 8, v145
	v_lshl_or_b32 v136, s70, 8, v146
	s_andn2_b64 vcc, exec, s[4:5]
	s_mov_b64 s[4:5], -1
	v_lshl_add_u32 v134, v138, 11, v136
	v_lshlrev_b32_e32 v135, 2, v134
	v_lshlrev_b32_e32 v137, 1, v134
	v_mov_b32_e32 v152, v135
	global_load_dwordx4 v[164:167], v152, s[36:37] nt
	global_load_dwordx4 v[168:171], v152, s[36:37] offset:16 nt
	global_load_dwordx4 v[172:175], v152, s[36:37] offset:512 nt
	global_load_dwordx4 v[176:179], v152, s[36:37] offset:528 nt
	v_add_u32_e32 v153, 0x20000, v135
	global_load_dwordx4 v[180:183], v153, s[36:37] nt
	global_load_dwordx4 v[184:187], v153, s[36:37] offset:16 nt
	global_load_dwordx4 v[188:191], v153, s[36:37] offset:512 nt
	global_load_dwordx4 v[192:195], v153, s[36:37] offset:528 nt
	v_add_u32_e32 v154, 0x40000, v135
	global_load_dwordx4 v[198:201], v154, s[36:37] nt
	global_load_dwordx4 v[202:205], v154, s[36:37] offset:16 nt
	global_load_dwordx4 v[206:209], v154, s[36:37] offset:512 nt
	global_load_dwordx4 v[210:213], v154, s[36:37] offset:528 nt
	s_waitcnt vmcnt(10)
	v_pk_add_f32 v[126:127], v[126:127], v[164:165]
	v_pk_add_f32 v[128:129], v[128:129], v[166:167]
	v_pk_add_f32 v[122:123], v[122:123], v[168:169]
	v_pk_add_f32 v[124:125], v[124:125], v[170:171]
	v_mov_b32_e32 v160, v137
	v_cvt_pk_bf16_f32 v126, v126, v127
	v_cvt_pk_bf16_f32 v127, v128, v129
	v_cvt_pk_bf16_f32 v128, v122, v123
	v_cvt_pk_bf16_f32 v129, v124, v125
	global_store_dwordx4 v160, v[126:129], s[12:13]
	v_add_u32_e32 v155, 0x60000, v135
	global_load_dwordx4 v[164:167], v155, s[36:37] nt
	global_load_dwordx4 v[168:171], v155, s[36:37] offset:16 nt
	s_waitcnt vmcnt(11)
	v_pk_add_f32 v[118:119], v[118:119], v[172:173]
	v_pk_add_f32 v[120:121], v[120:121], v[174:175]
	v_pk_add_f32 v[114:115], v[114:115], v[176:177]
	v_pk_add_f32 v[116:117], v[116:117], v[178:179]
	v_mov_b32_e32 v161, v137
	v_cvt_pk_bf16_f32 v118, v118, v119
	v_cvt_pk_bf16_f32 v119, v120, v121
	v_cvt_pk_bf16_f32 v120, v114, v115
	v_cvt_pk_bf16_f32 v121, v116, v117
	global_store_dwordx4 v161, v[118:121], s[12:13] offset:256
	global_load_dwordx4 v[172:175], v155, s[36:37] offset:512 nt
	global_load_dwordx4 v[176:179], v155, s[36:37] offset:528 nt
	s_waitcnt vmcnt(12)
	v_pk_add_f32 v[110:111], v[110:111], v[180:181]
	v_pk_add_f32 v[112:113], v[112:113], v[182:183]
	v_pk_add_f32 v[106:107], v[106:107], v[184:185]
	v_pk_add_f32 v[108:109], v[108:109], v[186:187]
	v_add_u32_e32 v160, 0x10000, v137
	v_cvt_pk_bf16_f32 v110, v110, v111
	v_cvt_pk_bf16_f32 v111, v112, v113
	v_cvt_pk_bf16_f32 v112, v106, v107
	v_cvt_pk_bf16_f32 v113, v108, v109
	global_store_dwordx4 v160, v[110:113], s[12:13]
	v_add_u32_e32 v156, 0x100000, v135
	global_load_dwordx4 v[180:183], v156, s[36:37] nt
	global_load_dwordx4 v[184:187], v156, s[36:37] offset:16 nt
	s_waitcnt vmcnt(13)
	v_pk_add_f32 v[102:103], v[102:103], v[188:189]
	v_pk_add_f32 v[104:105], v[104:105], v[190:191]
	v_pk_add_f32 v[98:99], v[98:99], v[192:193]
	v_pk_add_f32 v[100:101], v[100:101], v[194:195]
	v_add_u32_e32 v161, 0x10000, v137
	v_cvt_pk_bf16_f32 v102, v102, v103
	v_cvt_pk_bf16_f32 v103, v104, v105
	v_cvt_pk_bf16_f32 v104, v98, v99
	v_cvt_pk_bf16_f32 v105, v100, v101
	global_store_dwordx4 v161, v[102:105], s[12:13] offset:256
	global_load_dwordx4 v[188:191], v156, s[36:37] offset:512 nt
	global_load_dwordx4 v[192:195], v156, s[36:37] offset:528 nt
	s_waitcnt vmcnt(14)
	v_pk_add_f32 v[94:95], v[94:95], v[198:199]
	v_pk_add_f32 v[96:97], v[96:97], v[200:201]
	v_pk_add_f32 v[90:91], v[90:91], v[202:203]
	v_pk_add_f32 v[92:93], v[92:93], v[204:205]
	v_add_u32_e32 v160, 0x20000, v137
	v_cvt_pk_bf16_f32 v94, v94, v95
	v_cvt_pk_bf16_f32 v95, v96, v97
	v_cvt_pk_bf16_f32 v96, v90, v91
	v_cvt_pk_bf16_f32 v97, v92, v93
	global_store_dwordx4 v160, v[94:97], s[12:13]
	v_add_u32_e32 v157, 0x120000, v135
	global_load_dwordx4 v[198:201], v157, s[36:37] nt
	global_load_dwordx4 v[202:205], v157, s[36:37] offset:16 nt
	s_waitcnt vmcnt(15)
	v_pk_add_f32 v[86:87], v[86:87], v[206:207]
	v_pk_add_f32 v[88:89], v[88:89], v[208:209]
	v_pk_add_f32 v[82:83], v[82:83], v[210:211]
	v_pk_add_f32 v[84:85], v[84:85], v[212:213]
	v_add_u32_e32 v161, 0x20000, v137
	v_cvt_pk_bf16_f32 v86, v86, v87
	v_cvt_pk_bf16_f32 v87, v88, v89
	v_cvt_pk_bf16_f32 v88, v82, v83
	v_cvt_pk_bf16_f32 v89, v84, v85
	global_store_dwordx4 v161, v[86:89], s[12:13] offset:256
	global_load_dwordx4 v[206:209], v157, s[36:37] offset:512 nt
	global_load_dwordx4 v[210:213], v157, s[36:37] offset:528 nt
	s_waitcnt vmcnt(15)
	v_pk_add_f32 v[78:79], v[78:79], v[164:165]
	v_pk_add_f32 v[80:81], v[80:81], v[166:167]
	v_pk_add_f32 v[74:75], v[74:75], v[168:169]
	v_pk_add_f32 v[76:77], v[76:77], v[170:171]
	v_add_u32_e32 v160, 0x30000, v137
	v_cvt_pk_bf16_f32 v78, v78, v79
	v_cvt_pk_bf16_f32 v79, v80, v81
	v_cvt_pk_bf16_f32 v80, v74, v75
	v_cvt_pk_bf16_f32 v81, v76, v77
	global_store_dwordx4 v160, v[78:81], s[12:13]
	v_add_u32_e32 v158, 0x140000, v135
	global_load_dwordx4 v[164:167], v158, s[36:37] nt
	global_load_dwordx4 v[168:171], v158, s[36:37] offset:16 nt
	s_waitcnt vmcnt(15)
	v_pk_add_f32 v[70:71], v[70:71], v[172:173]
	v_pk_add_f32 v[72:73], v[72:73], v[174:175]
	v_pk_add_f32 v[66:67], v[66:67], v[176:177]
	v_pk_add_f32 v[68:69], v[68:69], v[178:179]
	v_add_u32_e32 v161, 0x30000, v137
	v_cvt_pk_bf16_f32 v70, v70, v71
	v_cvt_pk_bf16_f32 v71, v72, v73
	v_cvt_pk_bf16_f32 v72, v66, v67
	v_cvt_pk_bf16_f32 v73, v68, v69
	global_store_dwordx4 v161, v[70:73], s[12:13] offset:256
	global_load_dwordx4 v[172:175], v158, s[36:37] offset:512 nt
	global_load_dwordx4 v[176:179], v158, s[36:37] offset:528 nt
	s_waitcnt vmcnt(15)
	v_pk_add_f32 v[62:63], v[62:63], v[180:181]
	v_pk_add_f32 v[64:65], v[64:65], v[182:183]
	v_pk_add_f32 v[58:59], v[58:59], v[184:185]
	v_pk_add_f32 v[60:61], v[60:61], v[186:187]
	v_add_u32_e32 v160, 0x80000, v137
	v_cvt_pk_bf16_f32 v62, v62, v63
	v_cvt_pk_bf16_f32 v63, v64, v65
	v_cvt_pk_bf16_f32 v64, v58, v59
	v_cvt_pk_bf16_f32 v65, v60, v61
	global_store_dwordx4 v160, v[62:65], s[12:13]
	v_add_u32_e32 v159, 0x160000, v135
	global_load_dwordx4 v[180:183], v159, s[36:37] nt
	global_load_dwordx4 v[184:187], v159, s[36:37] offset:16 nt
	s_waitcnt vmcnt(15)
	v_pk_add_f32 v[54:55], v[54:55], v[188:189]
	v_pk_add_f32 v[56:57], v[56:57], v[190:191]
	v_pk_add_f32 v[50:51], v[50:51], v[192:193]
	v_pk_add_f32 v[52:53], v[52:53], v[194:195]
	v_add_u32_e32 v161, 0x80000, v137
	v_cvt_pk_bf16_f32 v54, v54, v55
	v_cvt_pk_bf16_f32 v55, v56, v57
	v_cvt_pk_bf16_f32 v56, v50, v51
	v_cvt_pk_bf16_f32 v57, v52, v53
	global_store_dwordx4 v161, v[54:57], s[12:13] offset:256
	global_load_dwordx4 v[188:191], v159, s[36:37] offset:512 nt
	global_load_dwordx4 v[192:195], v159, s[36:37] offset:528 nt
	s_waitcnt vmcnt(15)
	v_pk_add_f32 v[46:47], v[46:47], v[198:199]
	v_pk_add_f32 v[48:49], v[48:49], v[200:201]
	v_pk_add_f32 v[42:43], v[42:43], v[202:203]
	v_pk_add_f32 v[44:45], v[44:45], v[204:205]
	v_add_u32_e32 v160, 0x90000, v137
	v_cvt_pk_bf16_f32 v46, v46, v47
	v_cvt_pk_bf16_f32 v47, v48, v49
	v_cvt_pk_bf16_f32 v48, v42, v43
	v_cvt_pk_bf16_f32 v49, v44, v45
	global_store_dwordx4 v160, v[46:49], s[12:13]
	s_waitcnt vmcnt(13)
	v_pk_add_f32 v[30:31], v[30:31], v[206:207]
	v_pk_add_f32 v[32:33], v[32:33], v[208:209]
	v_pk_add_f32 v[26:27], v[26:27], v[210:211]
	v_pk_add_f32 v[28:29], v[28:29], v[212:213]
	v_add_u32_e32 v161, 0x90000, v137
	v_cvt_pk_bf16_f32 v30, v30, v31
	v_cvt_pk_bf16_f32 v31, v32, v33
	v_cvt_pk_bf16_f32 v32, v26, v27
	v_cvt_pk_bf16_f32 v33, v28, v29
	global_store_dwordx4 v161, v[30:33], s[12:13] offset:256
	s_waitcnt vmcnt(11)
	v_pk_add_f32 v[22:23], v[22:23], v[164:165]
	v_pk_add_f32 v[24:25], v[24:25], v[166:167]
	v_pk_add_f32 v[18:19], v[18:19], v[168:169]
	v_pk_add_f32 v[20:21], v[20:21], v[170:171]
	v_add_u32_e32 v160, 0xa0000, v137
	v_cvt_pk_bf16_f32 v22, v22, v23
	v_cvt_pk_bf16_f32 v23, v24, v25
	v_cvt_pk_bf16_f32 v24, v18, v19
	v_cvt_pk_bf16_f32 v25, v20, v21
	global_store_dwordx4 v160, v[22:25], s[12:13]
	s_waitcnt vmcnt(9)
	v_pk_add_f32 v[34:35], v[34:35], v[172:173]
	v_pk_add_f32 v[36:37], v[36:37], v[174:175]
	v_pk_add_f32 v[38:39], v[38:39], v[176:177]
	v_pk_add_f32 v[40:41], v[40:41], v[178:179]
	v_add_u32_e32 v161, 0xa0000, v137
	v_cvt_pk_bf16_f32 v34, v34, v35
	v_cvt_pk_bf16_f32 v35, v36, v37
	v_cvt_pk_bf16_f32 v36, v38, v39
	v_cvt_pk_bf16_f32 v37, v40, v41
	global_store_dwordx4 v161, v[34:37], s[12:13] offset:256
	s_waitcnt vmcnt(7)
	v_pk_add_f32 v[6:7], v[6:7], v[180:181]
	v_pk_add_f32 v[8:9], v[8:9], v[182:183]
	v_pk_add_f32 v[2:3], v[2:3], v[184:185]
	v_pk_add_f32 v[4:5], v[4:5], v[186:187]
	v_add_u32_e32 v160, 0xb0000, v137
	v_cvt_pk_bf16_f32 v6, v6, v7
	v_cvt_pk_bf16_f32 v7, v8, v9
	v_cvt_pk_bf16_f32 v8, v2, v3
	v_cvt_pk_bf16_f32 v9, v4, v5
	global_store_dwordx4 v160, v[6:9], s[12:13]
	s_waitcnt vmcnt(5)
	v_pk_add_f32 v[10:11], v[10:11], v[188:189]
	v_pk_add_f32 v[12:13], v[12:13], v[190:191]
	v_pk_add_f32 v[14:15], v[14:15], v[192:193]
	v_pk_add_f32 v[16:17], v[16:17], v[194:195]
	v_add_u32_e32 v161, 0xb0000, v137
	v_cvt_pk_bf16_f32 v10, v10, v11
	v_cvt_pk_bf16_f32 v11, v12, v13
	v_cvt_pk_bf16_f32 v12, v14, v15
	v_cvt_pk_bf16_f32 v13, v16, v17
	global_store_dwordx4 v161, v[10:13], s[12:13] offset:256
	s_cbranch_vccnz .LBB0_514
	s_andn2_b64 vcc, exec, s[0:1]
	s_cbranch_vccnz .LBB0_513
	s_barrier
	s_branch .LBB0_513
